# packed f32 adds for 1+2^z; batched LDS atomics in the prologue placement (fast path); early fetch of W1s/b1s
# speedup vs baseline: 1.0950x; 1.0164x over previous
.LBB1_39:
	s_or_b64 exec, exec, s[0:1]
	s_waitcnt lgkmcnt(0)
	s_barrier
	v_and_b32_e32 v120, 31, v0
	v_lshlrev_b32_e32 v120, 2, v120
	global_load_dword v108, v120, s[44:45]
	global_load_dword v109, v120, s[44:45] offset:512
	global_load_dword v110, v120, s[46:47]
	global_load_dword v111, v120, s[44:45] offset:128
	global_load_dword v112, v120, s[46:47] offset:128
	global_load_dword v113, v120, s[44:45] offset:256
	global_load_dword v114, v120, s[44:45] offset:768
	global_load_dword v115, v120, s[46:47] offset:256
	global_load_dword v116, v120, s[44:45] offset:640
	global_load_dword v117, v120, s[44:45] offset:384
	global_load_dword v118, v120, s[44:45] offset:896
	global_load_dword v119, v120, s[46:47] offset:384
	ds_read_b128 v[2:5], v62
	v_mbcnt_lo_u32_b32 v6, -1, 0
	v_mbcnt_hi_u32_b32 v6, -1, v6
	v_add_u32_e32 v8, -1, v6
	v_add_u32_e32 v11, -2, v6
	s_waitcnt lgkmcnt(0)
	v_add_u32_e32 v7, v3, v2
	v_add3_u32 v5, v7, v4, v5
	v_and_b32_e32 v7, 64, v6
	v_cmp_lt_i32_e32 vcc, v8, v7
	s_nop 1
	v_cndmask_b32_e32 v8, v8, v6, vcc
	v_lshlrev_b32_e32 v8, 2, v8
	ds_bpermute_b32 v9, v8, v5
	v_and_b32_e32 v8, 63, v0
	v_cmp_ne_u32_e32 vcc, 0, v8
	v_cmp_gt_u32_e64 s[0:1], 32, v8
	s_waitcnt lgkmcnt(0)
	v_cndmask_b32_e32 v9, 0, v9, vcc
	v_cmp_lt_i32_e32 vcc, v11, v7
	v_add_u32_e32 v9, v9, v5
	s_nop 0
	v_cndmask_b32_e32 v11, v11, v6, vcc
	v_lshlrev_b32_e32 v11, 2, v11
	ds_bpermute_b32 v11, v11, v9
	v_cmp_lt_u32_e32 vcc, 1, v8
	s_waitcnt lgkmcnt(0)
	s_nop 0
	v_cndmask_b32_e32 v11, 0, v11, vcc
	v_add_u32_e32 v9, v11, v9
	v_add_u32_e32 v11, -4, v6
	v_cmp_lt_i32_e32 vcc, v11, v7
	s_nop 1
	v_cndmask_b32_e32 v11, v11, v6, vcc
	v_lshlrev_b32_e32 v11, 2, v11
	ds_bpermute_b32 v11, v11, v9
	v_cmp_lt_u32_e32 vcc, 3, v8
	s_waitcnt lgkmcnt(0)
	s_nop 0
	v_cndmask_b32_e32 v11, 0, v11, vcc
	v_add_u32_e32 v9, v11, v9
	v_add_u32_e32 v11, -8, v6
	v_cmp_lt_i32_e32 vcc, v11, v7
	s_nop 1
	v_cndmask_b32_e32 v11, v11, v6, vcc
	v_lshlrev_b32_e32 v11, 2, v11
	ds_bpermute_b32 v11, v11, v9
	v_cmp_lt_u32_e32 vcc, 7, v8
	s_waitcnt lgkmcnt(0)
	s_nop 0
	v_cndmask_b32_e32 v11, 0, v11, vcc
	v_add_u32_e32 v9, v11, v9
	v_add_u32_e32 v11, -16, v6
	v_cmp_lt_i32_e32 vcc, v11, v7
	s_nop 1
	v_cndmask_b32_e32 v11, v11, v6, vcc
	v_lshlrev_b32_e32 v11, 2, v11
	ds_bpermute_b32 v11, v11, v9
	v_cmp_lt_u32_e32 vcc, 15, v8
	s_waitcnt lgkmcnt(0)
	s_nop 0
	v_cndmask_b32_e32 v11, 0, v11, vcc
	v_add_u32_e32 v11, v11, v9
	v_subrev_u32_e32 v9, 32, v6
	v_cmp_lt_i32_e32 vcc, v9, v7
	s_nop 1
	v_cndmask_b32_e32 v9, v9, v6, vcc
	v_lshlrev_b32_e32 v9, 2, v9
	ds_bpermute_b32 v14, v9, v11
	v_lshrrev_b32_e32 v9, 6, v0
	v_cmp_eq_u32_e32 vcc, 63, v8
	s_waitcnt lgkmcnt(0)
	v_cndmask_b32_e64 v14, v14, 0, s[0:1]
	v_add_u32_e32 v11, v14, v11
	s_and_saveexec_b64 s[4:5], vcc
	v_mov_b32_e32 v14, 0x16820
	v_lshl_or_b32 v14, v9, 2, v14
	ds_write_b32 v14, v11
	s_or_b64 exec, exec, s[4:5]
	v_mov_b32_e32 v14, 0x16820
	s_waitcnt lgkmcnt(0)
	s_barrier
	ds_read_b128 v[66:69], v14
	v_mov_b32_e32 v14, 0x16830
	ds_read_b128 v[70:73], v14
	v_cmp_lt_u32_e32 vcc, 63, v0
	s_movk_i32 s3, 0x7f
	s_waitcnt lgkmcnt(1)
	v_cndmask_b32_e32 v14, 0, v66, vcc
	v_cmp_lt_u32_e32 vcc, s3, v0
	s_movk_i32 s3, 0xbf
	s_nop 0
	v_cndmask_b32_e32 v16, 0, v67, vcc
	v_cmp_lt_u32_e32 vcc, s3, v0
	s_movk_i32 s3, 0xff
	s_nop 0
	v_cndmask_b32_e32 v66, 0, v68, vcc
	v_cmp_lt_u32_e32 vcc, s3, v0
	s_movk_i32 s3, 0x13f
	v_add3_u32 v14, v14, v16, v66
	v_cndmask_b32_e32 v16, 0, v69, vcc
	v_cmp_lt_u32_e32 vcc, s3, v0
	s_movk_i32 s3, 0x17f
	s_waitcnt lgkmcnt(0)
	v_cndmask_b32_e32 v66, 0, v70, vcc
	v_cmp_lt_u32_e32 vcc, s3, v0
	s_movk_i32 s3, 0x1bf
	v_add3_u32 v14, v14, v16, v66
	v_cndmask_b32_e32 v16, 0, v71, vcc
	v_cmp_lt_u32_e32 vcc, s3, v0
	s_movk_i32 s3, 0x1ff
	s_nop 0
	v_cndmask_b32_e32 v66, 0, v72, vcc
	v_cmp_lt_u32_e32 vcc, s3, v0
	v_add3_u32 v14, v14, v16, v66
	s_nop 0
	v_cndmask_b32_e32 v16, 0, v73, vcc
	v_add3_u32 v11, v14, v16, v11
	v_sub_u32_e32 v66, v11, v5
	v_add_u32_e32 v67, v66, v2
	v_add_u32_e32 v68, v67, v3
	v_mov_b32_e32 v2, 0x12810
	v_add_u32_e32 v69, v68, v4
	v_lshl_add_u32 v2, v0, 4, v2
	v_cmp_eq_u32_e32 vcc, s3, v0
	ds_write_b128 v2, v[66:69]
	ds_write_b128 v62, v[66:69]
	s_and_saveexec_b64 s[4:5], vcc
	v_mov_b32_e32 v2, 0x14810
	ds_write_b32 v2, v11
	s_or_b64 exec, exec, s[4:5]
	v_mov_b32_e32 v2, 0x14810
	s_waitcnt lgkmcnt(0)
	s_barrier
	ds_read_b32 v16, v2
	s_waitcnt lgkmcnt(0)
	v_readfirstlane_b32 s3, v16
	s_cmpk_lt_i32 s3, 0x1401
	s_cselect_b64 s[4:5], -1, 0
	s_cmpk_gt_i32 s3, 0x1400
	s_cselect_b64 s[60:61], -1, 0
	s_and_b64 vcc, exec, s[4:5]
	s_cbranch_vccnz .LBB1_49
	v_cmp_eq_u32_e32 vcc, 0, v0
	s_and_saveexec_b64 s[62:63], vcc
	s_cbranch_execz .LBB1_48
	s_mov_b64 s[66:67], exec
	v_mbcnt_lo_u32_b32 v3, s66, 0
	v_mbcnt_hi_u32_b32 v3, s67, v3
	v_add_u32_e32 v2, 0x60, v16
	v_cmp_eq_u32_e32 vcc, 0, v3
	s_and_saveexec_b64 s[64:65], vcc
	s_cbranch_execz .LBB1_47
	s_bcnt1_i32_b64 s3, s[66:67]
	v_mul_lo_u32 v4, v2, s3
	v_mov_b32_e32 v5, 0
	global_atomic_add v4, v5, v4, s[58:59] sc0

.LBB1_49:
	v_mov_b32_e32 v2, 0x16840
	v_mov_b32_e32 v3, 0x12800
	ds_read_b32 v14, v2
	ds_read_b32 v11, v3
	s_load_dword s33, s[48:49], 0x0
	s_and_b64 vcc, exec, s[60:61]
	s_cbranch_vccnz .Lplace_slow
	v_mov_b32_e32 v3, 1
	s_mov_b64 exec, s[28:29]
	v_and_b32_e32 v100, 0x1fffc, v65
	v_add_u32_e32 v100, 0x14820, v100
	ds_add_rtn_u32 v100, v100, v3
	s_mov_b64 exec, s[38:39]
	v_and_b32_e32 v101, 0x1fffc, v64
	v_add_u32_e32 v101, 0x14820, v101
	ds_add_rtn_u32 v101, v101, v3
	s_mov_b64 exec, s[36:37]
	v_and_b32_e32 v102, 0x1fffc, v63
	v_add_u32_e32 v102, 0x14820, v102
	ds_add_rtn_u32 v102, v102, v3
	s_mov_b64 exec, s[34:35]
	v_and_b32_e32 v103, 0x1fffc, v61
	v_add_u32_e32 v103, 0x14820, v103
	ds_add_rtn_u32 v103, v103, v3
	s_mov_b64 exec, s[30:31]
	v_and_b32_e32 v104, 0x1fffc, v60
	v_add_u32_e32 v104, 0x14820, v104
	ds_add_rtn_u32 v104, v104, v3
	s_mov_b64 exec, s[26:27]
	v_and_b32_e32 v105, 0x1fffc, v59
	v_add_u32_e32 v105, 0x14820, v105
	ds_add_rtn_u32 v105, v105, v3
	s_mov_b64 exec, s[24:25]
	v_and_b32_e32 v106, 0x1fffc, v58
	v_add_u32_e32 v106, 0x14820, v106
	ds_add_rtn_u32 v106, v106, v3
	s_mov_b64 exec, s[22:23]
	v_and_b32_e32 v107, 0x1fffc, v57
	v_add_u32_e32 v107, 0x14820, v107
	ds_add_rtn_u32 v107, v107, v3
	s_waitcnt lgkmcnt(0)
	s_mov_b64 exec, s[28:29]
	v_and_b32_e32 v50, 0x1ffff, v50
	v_lshlrev_b32_e32 v100, 3, v100
	ds_write_b64 v100, v[50:51]
	s_mov_b64 exec, s[38:39]
	v_and_b32_e32 v48, 0x1ffff, v48
	v_lshlrev_b32_e32 v101, 3, v101
	ds_write_b64 v101, v[48:49]
	s_mov_b64 exec, s[36:37]
	v_and_b32_e32 v46, 0x1ffff, v46
	v_lshlrev_b32_e32 v102, 3, v102
	ds_write_b64 v102, v[46:47]
	s_mov_b64 exec, s[34:35]
	v_and_b32_e32 v44, 0x1ffff, v44
	v_lshlrev_b32_e32 v103, 3, v103
	ds_write_b64 v103, v[44:45]
	s_mov_b64 exec, s[30:31]
	v_and_b32_e32 v42, 0x1ffff, v42
	v_lshlrev_b32_e32 v104, 3, v104
	ds_write_b64 v104, v[42:43]
	s_mov_b64 exec, s[26:27]
	v_and_b32_e32 v40, 0x1ffff, v40
	v_lshlrev_b32_e32 v105, 3, v105
	ds_write_b64 v105, v[40:41]
	s_mov_b64 exec, s[24:25]
	v_and_b32_e32 v38, 0x1ffff, v38
	v_lshlrev_b32_e32 v106, 3, v106
	ds_write_b64 v106, v[38:39]
	s_mov_b64 exec, s[22:23]
	v_and_b32_e32 v36, 0x1ffff, v36
	v_lshlrev_b32_e32 v107, 3, v107
	ds_write_b64 v107, v[36:37]
	s_waitcnt lgkmcnt(0)
	s_mov_b64 exec, s[20:21]
	v_and_b32_e32 v100, 0x1fffc, v56
	v_add_u32_e32 v100, 0x14820, v100
	ds_add_rtn_u32 v100, v100, v3
	s_mov_b64 exec, s[18:19]
	v_and_b32_e32 v101, 0x1fffc, v55
	v_add_u32_e32 v101, 0x14820, v101
	ds_add_rtn_u32 v101, v101, v3
	s_mov_b64 exec, s[16:17]
	v_and_b32_e32 v102, 0x1fffc, v54
	v_add_u32_e32 v102, 0x14820, v102
	ds_add_rtn_u32 v102, v102, v3
	s_mov_b64 exec, s[14:15]
	v_and_b32_e32 v103, 0x1fffc, v52
	v_add_u32_e32 v103, 0x14820, v103
	ds_add_rtn_u32 v103, v103, v3
	s_mov_b64 exec, s[12:13]
	v_and_b32_e32 v104, 0x1fffc, v17
	v_add_u32_e32 v104, 0x14820, v104
	ds_add_rtn_u32 v104, v104, v3
	s_mov_b64 exec, s[10:11]
	v_and_b32_e32 v105, 0x1fffc, v15
	v_add_u32_e32 v105, 0x14820, v105
	ds_add_rtn_u32 v105, v105, v3
	s_mov_b64 exec, s[8:9]
	v_and_b32_e32 v106, 0x1fffc, v13
	v_add_u32_e32 v106, 0x14820, v106
	ds_add_rtn_u32 v106, v106, v3
	s_mov_b64 exec, s[6:7]
	v_and_b32_e32 v107, 0x1fffc, v12
	v_add_u32_e32 v107, 0x14820, v107
	ds_add_rtn_u32 v107, v107, v3
	s_waitcnt lgkmcnt(0)
	s_mov_b64 exec, s[20:21]
	v_and_b32_e32 v34, 0x1ffff, v34
	v_lshlrev_b32_e32 v100, 3, v100
	ds_write_b64 v100, v[34:35]
	s_mov_b64 exec, s[18:19]
	v_and_b32_e32 v32, 0x1ffff, v32
	v_lshlrev_b32_e32 v101, 3, v101
	ds_write_b64 v101, v[32:33]
	s_mov_b64 exec, s[16:17]
	v_and_b32_e32 v30, 0x1ffff, v30
	v_lshlrev_b32_e32 v102, 3, v102
	ds_write_b64 v102, v[30:31]
	s_mov_b64 exec, s[14:15]
	v_and_b32_e32 v28, 0x1ffff, v28
	v_lshlrev_b32_e32 v103, 3, v103
	ds_write_b64 v103, v[28:29]
	s_mov_b64 exec, s[12:13]
	v_and_b32_e32 v26, 0x1ffff, v26
	v_lshlrev_b32_e32 v104, 3, v104
	ds_write_b64 v104, v[26:27]
	s_mov_b64 exec, s[10:11]
	v_and_b32_e32 v24, 0x1ffff, v24
	v_lshlrev_b32_e32 v105, 3, v105
	ds_write_b64 v105, v[24:25]
	s_mov_b64 exec, s[8:9]
	v_and_b32_e32 v22, 0x1ffff, v22
	v_lshlrev_b32_e32 v106, 3, v106
	ds_write_b64 v106, v[22:23]
	s_mov_b64 exec, s[6:7]
	v_and_b32_e32 v20, 0x1ffff, v20
	v_lshlrev_b32_e32 v107, 3, v107
	ds_write_b64 v107, v[20:21]
	s_mov_b64 exec, -1
	s_branch .Lplace_join
.Lplace_slow:
	s_and_saveexec_b64 s[48:49], s[28:29]
	s_cbranch_execz .LBB1_54
	v_and_b32_e32 v2, 0x1fffc, v65
	v_add_u32_e32 v2, 0x14820, v2
	v_mov_b32_e32 v3, 1
	ds_add_rtn_u32 v2, v2, v3
	v_and_b32_e32 v50, 0x1ffff, v50
	s_mov_b64 s[28:29], -1
	s_and_b64 vcc, exec, s[60:61]
	s_cbranch_vccz .LBB1_52
	s_waitcnt lgkmcnt(0)
	v_add_u32_e32 v4, v2, v14
	v_ashrrev_i32_e32 v5, 31, v4
	v_lshl_add_u64 v[4:5], v[4:5], 3, s[56:57]
	global_store_dwordx2 v[4:5], v[50:51], off
	s_mov_b64 s[28:29], 0

.Lplace_join:
	s_and_saveexec_b64 s[6:7], s[40:41]
	s_cbranch_execz .LBB1_136
	s_waitcnt lgkmcnt(0)
	v_lshlrev_b32_e32 v2, 3, v53
	v_mov_b32_e32 v3, 0
	v_lshl_add_u64 v[2:3], v[18:19], 3, v[2:3]
	v_lshl_add_u64 v[2:3], s[42:43], 0, v[2:3]
	s_mov_b64 s[8:9], 0x100
	v_lshl_add_u64 v[2:3], v[2:3], 0, s[8:9]
	s_mov_b64 s[8:9], 0
	v_mov_b32_e32 v12, 1
	s_branch .LBB1_132

.Lstag_done:
	v_lshlrev_b32_e32 v3, 2, v22
	s_waitcnt vmcnt(0)
	v_mov_b32_e32 v18, v108
	v_mov_b32_e32 v19, v109
	v_mov_b32_e32 v20, v110
	v_mov_b32_e32 v16, v111
	v_mov_b32_e32 v17, v112
	v_mov_b32_e32 v12, v113
	v_mov_b32_e32 v13, v114
	v_mov_b32_e32 v15, v115
	v_mov_b32_e32 v4, 0x180
	v_lshl_or_b32 v23, v8, 2, v4
	v_mov_b32_e32 v21, v116
	v_mov_b32_e32 v4, v117
	v_mov_b32_e32 v5, v118
	v_mov_b32_e32 v10, v119
	v_mov_b32_e32 v3, 0x12810
	v_lshl_add_u32 v23, v9, 10, v3
	ds_read2_b32 v[24:25], v23 offset1:32
	v_add_u32_e32 v2, v23, v2
	ds_read2_b32 v[230:231], v2 offset1:1
	v_lshlrev_b32_e32 v26, 8, v9
	s_lshl_b32 s2, s2, 11
	v_or3_b32 v235, v26, s2, v1
	s_mov_b32 s12, 0x7a120
	s_waitcnt lgkmcnt(1)
	v_readfirstlane_b32 s13, v24
	v_readfirstlane_b32 s6, v25
	v_cmp_gt_i32_e32 vcc, s12, v235
	v_mov_b32_e32 v2, 0
	v_mov_b32_e32 v238, 0
	s_and_saveexec_b64 s[2:3], vcc
	s_cbranch_execz .LBB1_143
	v_ashrrev_i32_e32 v25, 31, v235
	v_mov_b32_e32 v24, v235
	v_lshl_add_u64 v[24:25], v[24:25], 2, s[50:51]
	global_load_dword v238, v[24:25], off
.LBB1_143:
	s_or_b64 exec, exec, s[2:3]
	v_cndmask_b32_e64 v24, v14, 0, s[4:5]
	v_ashrrev_i32_e32 v25, 31, v24
	v_lshlrev_b64 v[24:25], 3, v[24:25]
	s_mov_b64 s[2:3], src_shared_base
	v_lshl_add_u64 v[24:25], s[56:57], 0, v[24:25]
	v_mov_b32_e32 v14, s3
	v_cndmask_b32_e64 v232, v24, 0, s[4:5]
	v_add_lshl_u32 v24, s13, v1, 1
	v_cndmask_b32_e64 v233, v25, v14, s[4:5]
	s_mov_b32 s81, s4
	v_ashrrev_i32_e32 v25, 31, v24
	v_lshl_add_u64 v[24:25], v[24:25], 2, v[232:233]
	flat_load_dwordx2 v[82:83], v[24:25]
	s_mov_b32 s2, 0x4038aa3b
	v_add_f32_e32 v239, s33, v11
	s_waitcnt vmcnt(0)
	v_fma_mixlo_f16 v11, v18, s2, 0
	v_fma_mixlo_f16 v25, v16, s2, 0
	v_fma_mixlo_f16 v27, v17, s2, 0
	v_add_lshl_u32 v22, s13, v22, 1
	v_fma_mixlo_f16 v14, v19, s2, 0
	v_fma_mixlo_f16 v18, v18, s2, -v11 op_sel_hi:[0,0,1]
	v_fma_mixlo_f16 v16, v16, s2, -v25 op_sel_hi:[0,0,1]
	v_fma_mixlo_f16 v17, v17, s2, -v27 op_sel_hi:[0,0,1]
	s_mov_b32 s14, 0x186a0
	v_ashrrev_i32_e32 v23, 31, v22
	v_fma_mixlo_f16 v19, v19, s2, -v14 op_sel_hi:[0,0,1]
	v_cndmask_b32_e64 v11, 0, v11, s[0:1]
	v_cndmask_b32_e64 v14, 0, v14, s[0:1]
	v_cndmask_b32_e64 v25, 0, v25, s[0:1]
	v_cndmask_b32_e64 v27, 0, v27, s[0:1]
	v_cndmask_b32_e64 v18, 0, v18, s[0:1]
	v_cndmask_b32_e64 v16, 0, v16, s[0:1]
	v_cndmask_b32_e64 v17, 0, v17, s[0:1]
	v_pack_b32_f16 v179, v11, v14
	v_pack_b32_f16 v178, v11, v18
	v_pack_b32_f16 v185, v27, v17
	v_pack_b32_f16 v182, v25, v16
	v_lshl_add_u64 v[16:17], v[22:23], 2, v[232:233]
	flat_load_dwordx2 v[236:237], v[16:17]
	v_mov_b32_e32 v17, v2
	v_cndmask_b32_e64 v19, 0, v19, s[0:1]
	v_pack_b32_f16 v180, v19, v14
	v_fma_mixlo_f16 v14, v13, s2, 0
	v_fma_mixlo_f16 v13, v13, s2, -v14 op_sel_hi:[0,0,1]
	v_cndmask_b32_e64 v14, 0, v14, s[0:1]
	v_cndmask_b32_e64 v13, 0, v13, s[0:1]
	v_fma_mixlo_f16 v24, v20, s2, 0
	v_fma_mixlo_f16 v26, v21, s2, 0
	v_or_b32_e32 v240, 64, v1
	v_pack_b32_f16 v188, v13, v14
	v_fma_mixlo_f16 v13, v10, s2, 0
	v_lshl_add_u32 v244, v1, 2, v3
	v_and_b32_e32 v0, 32, v0
	v_mov_b32_e32 v1, 0xa300
	v_fma_mixlo_f16 v20, v20, s2, -v24 op_sel_hi:[0,0,1]
	v_fma_mixlo_f16 v21, v21, s2, -v26 op_sel_hi:[0,0,1]
	v_fma_mixlo_f16 v10, v10, s2, -v13 op_sel_hi:[0,0,1]
	v_lshl_or_b32 v245, v0, 2, v1
	v_lshl_add_u32 v246, v8, 4, v1
	v_add_u32_e32 v3, 64, v7
	v_cndmask_b32_e64 v24, 0, v24, s[0:1]
	v_cndmask_b32_e64 v26, 0, v26, s[0:1]
	v_cndmask_b32_e64 v20, 0, v20, s[0:1]
	v_cndmask_b32_e64 v21, 0, v21, s[0:1]
	v_cndmask_b32_e64 v13, 0, v13, s[0:1]
	v_cndmask_b32_e64 v10, 0, v10, s[0:1]
	v_mov_b32_e32 v0, 0xc0
	v_pack_b32_f16 v183, v25, v26
	v_pack_b32_f16 v181, v24, v20
	v_pack_b32_f16 v184, v21, v26
	v_pack_b32_f16 v193, v13, v10
	v_lshlrev_b32_e32 v251, 3, v9
	v_mov_b32_e32 v7, v2
	v_mov_b32_e32 v9, v2
	v_mov_b32_e32 v10, v2
	v_mov_b32_e32 v13, v2
	v_add_u32_e32 v242, 8, v251
	s_waitcnt lgkmcnt(0)
	v_sub_u32_e32 v234, v231, v230
	s_mov_b64 s[4:5], 0
	v_mov_b32_e32 v249, s6
	v_mov_b32_e32 v231, s13
	s_mov_b32 s15, 0x5040100
	s_mov_b32 s82, 1.0
	s_mov_b32 s83, 1.0
	s_mov_b32 s73, 0x3c000000
	s_mov_b32 s74, 0x42004000
	s_mov_b32 s75, 0x48804800
	s_mov_b32 s76, 0x49804900
	s_mov_b32 s77, 0x4c404c00
	s_mov_b32 s78, 0x4cc04c80
	s_mov_b32 s79, 0x4e404e00
	s_mov_b32 s80, 0x4ec04e80
	v_mov_b32_e32 v197, 0x3c003c00
	s_mov_b32 s16, 0x10000
	s_mov_b32 s17, 0x7a100
	v_lshl_or_b32 v11, v82, 3, 3
	v_cmp_gt_u32_e32 vcc, s14, v82
	v_mov_b32_e32 v196, v83
	s_nop 0
	v_cndmask_b32_e32 v16, 3, v11, vcc
	v_lshl_add_u64 v[16:17], v[16:17], 2, s[54:55]
	global_load_dword v241, v[16:17], off
	v_fma_mixlo_f16 v11, v12, s2, 0
	v_fma_mixlo_f16 v12, v12, s2, -v11 op_sel_hi:[0,0,1]
	v_cndmask_b32_e64 v11, 0, v11, s[0:1]
	v_cndmask_b32_e64 v12, 0, v12, s[0:1]
	v_pack_b32_f16 v187, v11, v14
	v_pack_b32_f16 v186, v11, v12
	v_fma_mixlo_f16 v11, v4, s2, 0
	v_fma_mixlo_f16 v4, v4, s2, -v11 op_sel_hi:[0,0,1]
	v_cndmask_b32_e64 v11, 0, v11, s[0:1]
	v_cndmask_b32_e64 v4, 0, v4, s[0:1]
	v_fma_mixlo_f16 v16, v15, s2, 0
	v_pack_b32_f16 v190, v11, v4
	v_lshrrev_b32_e32 v4, 3, v8
	v_fma_mixlo_f16 v15, v15, s2, -v16 op_sel_hi:[0,0,1]
	v_fma_mixlo_f16 v12, v5, s2, 0
	v_and_b32_e32 v243, 4, v4
	v_cndmask_b32_e64 v16, 0, v16, s[0:1]
	v_cndmask_b32_e64 v15, 0, v15, s[0:1]
	v_fma_mixlo_f16 v5, v5, s2, -v12 op_sel_hi:[0,0,1]
	v_lshl_add_u32 v247, v243, 6, v1
	v_xor_b32_e32 v1, 32, v6
	v_pack_b32_f16 v189, v16, v15
	v_cndmask_b32_e64 v12, 0, v12, s[0:1]
	v_cndmask_b32_e64 v5, 0, v5, s[0:1]
	v_cmp_lt_i32_e32 vcc, v1, v3
	v_mov_b32_e32 v16, v2
	v_mov_b32_e32 v17, v2
	v_pack_b32_f16 v191, v11, v12
	v_pack_b32_f16 v192, v5, v12
	v_lshl_or_b32 v0, v4, 6, v0
	v_cndmask_b32_e32 v1, v6, v1, vcc
	v_mov_b32_e32 v3, v2
	v_mov_b32_e32 v4, v2
	v_mov_b32_e32 v5, v2
	v_mov_b32_e32 v6, v2
	v_mov_b32_e32 v8, v2
	v_mov_b32_e32 v11, v2
	v_mov_b32_e32 v12, v2
	v_mov_b32_e32 v14, v2
	v_mov_b32_e32 v15, v2
	v_mov_b64_e32 v[32:33], v[16:17]
	v_mov_b64_e32 v[48:49], v[16:17]
	v_mov_b64_e32 v[64:65], v[16:17]
	v_mov_b64_e32 v[80:81], v[16:17]
	v_lshlrev_b32_e32 v248, 2, v1
	v_add_u32_e32 v250, 0xa300, v0
	v_mov_b64_e32 v[30:31], v[14:15]
	v_mov_b64_e32 v[28:29], v[12:13]
	v_mov_b64_e32 v[26:27], v[10:11]
	v_mov_b64_e32 v[24:25], v[8:9]
	v_mov_b64_e32 v[22:23], v[6:7]
	v_mov_b64_e32 v[20:21], v[4:5]
	v_mov_b64_e32 v[18:19], v[2:3]
	v_mov_b64_e32 v[46:47], v[14:15]
	v_mov_b64_e32 v[44:45], v[12:13]
	v_mov_b64_e32 v[42:43], v[10:11]
	v_mov_b64_e32 v[40:41], v[8:9]
	v_mov_b64_e32 v[38:39], v[6:7]
	v_mov_b64_e32 v[36:37], v[4:5]
	v_mov_b64_e32 v[34:35], v[2:3]
	v_mov_b64_e32 v[62:63], v[14:15]
	v_mov_b64_e32 v[60:61], v[12:13]
	v_mov_b64_e32 v[58:59], v[10:11]
	v_mov_b64_e32 v[56:57], v[8:9]
	v_mov_b64_e32 v[54:55], v[6:7]
	v_mov_b64_e32 v[52:53], v[4:5]
	v_mov_b64_e32 v[50:51], v[2:3]
	v_mov_b64_e32 v[78:79], v[14:15]
	v_mov_b64_e32 v[76:77], v[12:13]
	v_mov_b64_e32 v[74:75], v[10:11]
	v_mov_b64_e32 v[72:73], v[8:9]
	v_mov_b64_e32 v[70:71], v[6:7]
	v_mov_b64_e32 v[68:69], v[4:5]
	v_mov_b64_e32 v[66:67], v[2:3]
	s_branch .LBB1_145

.Lcs_done:
	global_load_dword v241, v4, s[54:55]
	s_add_i32 s18, s13, 32
	s_add_i32 s19, s13, 16
	s_mov_b64 s[6:7], 0
	v_mfma_f32_32x32x16_f16 v[82:97], v[194:197], v[178:181], 0
	v_mfma_f32_32x32x16_f16 v[98:113], v[194:197], v[182:185], 0
	v_add_u32_e32 v14, s13, v243
	v_sub_u32_e32 v3, v230, v14
	v_add_u32_e32 v4, v3, v234
	v_add_u32_e32 v5, -1, v3
	v_med3_i32 v4, v4, -1, 32
	v_med3_i32 v5, v5, -1, 32
	v_cvt_f32_i32_e32 v4, v4
	v_cvt_f32_i32_e32 v5, v5
	v_cvt_pk_f16_f32 v14, v4, v4
	v_cvt_pk_f16_f32 v15, v5, v5
	v_pk_add_f16 v3, v14, s73 neg_lo:[0,1] neg_hi:[0,1]
	v_pk_add_f16 v4, s73, v15 neg_lo:[0,1] neg_hi:[0,1]
	v_pk_min_f16 v6, v3, v4 clamp
	v_pk_add_f16 v5, v14, s74 neg_lo:[0,1] neg_hi:[0,1]
	v_pk_add_f16 v16, s74, v15 neg_lo:[0,1] neg_hi:[0,1]
	v_pk_min_f16 v7, v5, v16 clamp
	v_pk_add_f16 v3, v14, s75 neg_lo:[0,1] neg_hi:[0,1]
	v_pk_add_f16 v4, s75, v15 neg_lo:[0,1] neg_hi:[0,1]
	v_pk_min_f16 v8, v3, v4 clamp
	v_pk_add_f16 v5, v14, s76 neg_lo:[0,1] neg_hi:[0,1]
	v_pk_add_f16 v16, s76, v15 neg_lo:[0,1] neg_hi:[0,1]
	v_pk_min_f16 v9, v5, v16 clamp
	v_pk_add_f16 v3, v14, s77 neg_lo:[0,1] neg_hi:[0,1]
	v_pk_add_f16 v4, s77, v15 neg_lo:[0,1] neg_hi:[0,1]
	v_pk_min_f16 v10, v3, v4 clamp
	v_pk_add_f16 v5, v14, s78 neg_lo:[0,1] neg_hi:[0,1]
	v_pk_add_f16 v16, s78, v15 neg_lo:[0,1] neg_hi:[0,1]
	v_pk_min_f16 v11, v5, v16 clamp
	v_pk_add_f16 v3, v14, s79 neg_lo:[0,1] neg_hi:[0,1]
	v_pk_add_f16 v4, s79, v15 neg_lo:[0,1] neg_hi:[0,1]
	v_pk_min_f16 v12, v3, v4 clamp
	v_pk_add_f16 v5, v14, s80 neg_lo:[0,1] neg_hi:[0,1]
	v_pk_add_f16 v16, s80, v15 neg_lo:[0,1] neg_hi:[0,1]
	v_pk_min_f16 v13, v5, v16 clamp
	v_exp_f32_e32 v82, v82
	v_exp_f32_e32 v83, v83
	v_exp_f32_e32 v84, v84
	v_exp_f32_e32 v85, v85
	v_exp_f32_e32 v86, v86
	v_exp_f32_e32 v87, v87
	v_exp_f32_e32 v88, v88
	v_exp_f32_e32 v89, v89
	v_exp_f32_e32 v90, v90
	v_exp_f32_e32 v91, v91
	v_exp_f32_e32 v92, v92
	v_exp_f32_e32 v93, v93
	v_exp_f32_e32 v94, v94
	v_exp_f32_e32 v95, v95
	v_exp_f32_e32 v96, v96
	v_exp_f32_e32 v97, v97
	v_pk_add_f32 v[82:83], v[82:83], s[82:83]
	v_pk_add_f32 v[84:85], v[84:85], s[82:83]
	v_pk_add_f32 v[86:87], v[86:87], s[82:83]
	v_pk_add_f32 v[88:89], v[88:89], s[82:83]
	v_pk_add_f32 v[90:91], v[90:91], s[82:83]
	v_pk_add_f32 v[92:93], v[92:93], s[82:83]
	v_pk_add_f32 v[94:95], v[94:95], s[82:83]
	v_pk_add_f32 v[96:97], v[96:97], s[82:83]
	v_rcp_f32_e32 v82, v82
	v_rcp_f32_e32 v83, v83
	v_rcp_f32_e32 v84, v84
	v_rcp_f32_e32 v85, v85
	v_rcp_f32_e32 v86, v86
	v_rcp_f32_e32 v87, v87
	v_rcp_f32_e32 v88, v88
	v_rcp_f32_e32 v89, v89
	v_rcp_f32_e32 v90, v90
	v_rcp_f32_e32 v91, v91
	v_rcp_f32_e32 v92, v92
	v_rcp_f32_e32 v93, v93
	v_rcp_f32_e32 v94, v94
	v_rcp_f32_e32 v95, v95
	v_rcp_f32_e32 v96, v96
	v_rcp_f32_e32 v97, v97
	v_cvt_pk_f16_f32 v198, v82, v83
	v_cvt_pk_f16_f32 v199, v84, v85
	v_cvt_pk_f16_f32 v200, v86, v87
	v_cvt_pk_f16_f32 v201, v88, v89
	v_cvt_pk_f16_f32 v202, v90, v91
	v_cvt_pk_f16_f32 v203, v92, v93
	v_cvt_pk_f16_f32 v204, v94, v95
	v_cvt_pk_f16_f32 v205, v96, v97
	v_mfma_f32_32x32x16_f16 v[82:97], v[194:197], v[186:189], 0
	v_exp_f32_e32 v98, v98
	v_exp_f32_e32 v99, v99
	v_exp_f32_e32 v100, v100
	v_exp_f32_e32 v101, v101
	v_exp_f32_e32 v102, v102
	v_exp_f32_e32 v103, v103
	v_mfma_f32_32x32x16_f16 v[66:81], v[198:201], v[6:9], v[66:81]
	v_exp_f32_e32 v104, v104
	v_exp_f32_e32 v105, v105
	v_exp_f32_e32 v106, v106
	v_exp_f32_e32 v107, v107
	v_exp_f32_e32 v108, v108
	v_exp_f32_e32 v109, v109
	v_mfma_f32_32x32x16_f16 v[66:81], v[202:205], v[10:13], v[66:81]
	v_exp_f32_e32 v110, v110
	v_exp_f32_e32 v111, v111
	v_exp_f32_e32 v112, v112
	v_exp_f32_e32 v113, v113
	v_pk_add_f32 v[98:99], v[98:99], s[82:83]
	v_pk_add_f32 v[100:101], v[100:101], s[82:83]
	v_pk_add_f32 v[102:103], v[102:103], s[82:83]
	v_pk_add_f32 v[104:105], v[104:105], s[82:83]
	v_pk_add_f32 v[106:107], v[106:107], s[82:83]
	v_pk_add_f32 v[108:109], v[108:109], s[82:83]
	v_pk_add_f32 v[110:111], v[110:111], s[82:83]
	v_pk_add_f32 v[112:113], v[112:113], s[82:83]
	v_rcp_f32_e32 v98, v98
	v_rcp_f32_e32 v99, v99
	v_rcp_f32_e32 v100, v100
	v_rcp_f32_e32 v101, v101
	v_rcp_f32_e32 v102, v102
	v_rcp_f32_e32 v103, v103
	v_rcp_f32_e32 v104, v104
	v_rcp_f32_e32 v105, v105
	v_rcp_f32_e32 v106, v106
	v_rcp_f32_e32 v107, v107
	v_rcp_f32_e32 v108, v108
	v_rcp_f32_e32 v109, v109
	v_rcp_f32_e32 v110, v110
	v_rcp_f32_e32 v111, v111
	v_rcp_f32_e32 v112, v112
	v_rcp_f32_e32 v113, v113
	v_cvt_pk_f16_f32 v206, v98, v99
	v_cvt_pk_f16_f32 v207, v100, v101
	v_cvt_pk_f16_f32 v208, v102, v103
	v_cvt_pk_f16_f32 v209, v104, v105
	v_cvt_pk_f16_f32 v210, v106, v107
	v_cvt_pk_f16_f32 v211, v108, v109
	v_cvt_pk_f16_f32 v212, v110, v111
	v_cvt_pk_f16_f32 v213, v112, v113
	v_mfma_f32_32x32x16_f16 v[98:113], v[194:197], v[190:193], 0
	v_exp_f32_e32 v82, v82
	v_exp_f32_e32 v83, v83
	v_exp_f32_e32 v84, v84
	v_exp_f32_e32 v85, v85
	v_exp_f32_e32 v86, v86
	v_exp_f32_e32 v87, v87
	v_mfma_f32_32x32x16_f16 v[50:65], v[206:209], v[6:9], v[50:65]
	v_exp_f32_e32 v88, v88
	v_exp_f32_e32 v89, v89
	v_exp_f32_e32 v90, v90
	v_exp_f32_e32 v91, v91
	v_exp_f32_e32 v92, v92
	v_exp_f32_e32 v93, v93
	v_mfma_f32_32x32x16_f16 v[50:65], v[210:213], v[10:13], v[50:65]
	v_exp_f32_e32 v94, v94
	v_exp_f32_e32 v95, v95
	v_exp_f32_e32 v96, v96
	v_exp_f32_e32 v97, v97
	v_pk_add_f32 v[82:83], v[82:83], s[82:83]
	v_pk_add_f32 v[84:85], v[84:85], s[82:83]
	v_pk_add_f32 v[86:87], v[86:87], s[82:83]
	v_pk_add_f32 v[88:89], v[88:89], s[82:83]
	v_pk_add_f32 v[90:91], v[90:91], s[82:83]
	v_pk_add_f32 v[92:93], v[92:93], s[82:83]
	v_pk_add_f32 v[94:95], v[94:95], s[82:83]
	v_pk_add_f32 v[96:97], v[96:97], s[82:83]
	v_rcp_f32_e32 v82, v82
	v_rcp_f32_e32 v83, v83
	v_rcp_f32_e32 v84, v84
	v_rcp_f32_e32 v85, v85
	v_rcp_f32_e32 v86, v86
	v_rcp_f32_e32 v87, v87
	v_rcp_f32_e32 v88, v88
	v_rcp_f32_e32 v89, v89
	v_rcp_f32_e32 v90, v90
	v_rcp_f32_e32 v91, v91
	v_rcp_f32_e32 v92, v92
	v_rcp_f32_e32 v93, v93
	v_rcp_f32_e32 v94, v94
	v_rcp_f32_e32 v95, v95
	v_rcp_f32_e32 v96, v96
	v_rcp_f32_e32 v97, v97
	v_cvt_pk_f16_f32 v214, v82, v83
	v_cvt_pk_f16_f32 v215, v84, v85
	v_cvt_pk_f16_f32 v216, v86, v87
	v_cvt_pk_f16_f32 v217, v88, v89
	v_cvt_pk_f16_f32 v218, v90, v91
	v_cvt_pk_f16_f32 v219, v92, v93
	v_cvt_pk_f16_f32 v220, v94, v95
	v_cvt_pk_f16_f32 v221, v96, v97
	v_exp_f32_e32 v98, v98
	v_exp_f32_e32 v99, v99
	v_exp_f32_e32 v100, v100
	v_exp_f32_e32 v101, v101
	v_exp_f32_e32 v102, v102
	v_exp_f32_e32 v103, v103
	v_mfma_f32_32x32x16_f16 v[34:49], v[214:217], v[6:9], v[34:49]
	v_exp_f32_e32 v104, v104
	v_exp_f32_e32 v105, v105
	v_exp_f32_e32 v106, v106
	v_exp_f32_e32 v107, v107
	v_exp_f32_e32 v108, v108
	v_exp_f32_e32 v109, v109
	v_mfma_f32_32x32x16_f16 v[34:49], v[218:221], v[10:13], v[34:49]
	v_exp_f32_e32 v110, v110
	v_exp_f32_e32 v111, v111
	v_exp_f32_e32 v112, v112
	v_exp_f32_e32 v113, v113
	v_pk_add_f32 v[98:99], v[98:99], s[82:83]
	v_pk_add_f32 v[100:101], v[100:101], s[82:83]
	v_pk_add_f32 v[102:103], v[102:103], s[82:83]
	v_pk_add_f32 v[104:105], v[104:105], s[82:83]
	v_pk_add_f32 v[106:107], v[106:107], s[82:83]
	v_pk_add_f32 v[108:109], v[108:109], s[82:83]
	v_pk_add_f32 v[110:111], v[110:111], s[82:83]
	v_pk_add_f32 v[112:113], v[112:113], s[82:83]
	v_rcp_f32_e32 v98, v98
	v_rcp_f32_e32 v99, v99
	v_rcp_f32_e32 v100, v100
	v_rcp_f32_e32 v101, v101
	v_rcp_f32_e32 v102, v102
	v_rcp_f32_e32 v103, v103
	v_rcp_f32_e32 v104, v104
	v_rcp_f32_e32 v105, v105
	v_rcp_f32_e32 v106, v106
	v_rcp_f32_e32 v107, v107
	v_rcp_f32_e32 v108, v108
	v_rcp_f32_e32 v109, v109
	v_rcp_f32_e32 v110, v110
	v_rcp_f32_e32 v111, v111
	v_rcp_f32_e32 v112, v112
	v_rcp_f32_e32 v113, v113
	v_cvt_pk_f16_f32 v222, v98, v99
	v_cvt_pk_f16_f32 v223, v100, v101
	v_cvt_pk_f16_f32 v224, v102, v103
	v_cvt_pk_f16_f32 v225, v104, v105
	v_cvt_pk_f16_f32 v226, v106, v107
	v_cvt_pk_f16_f32 v227, v108, v109
	v_cvt_pk_f16_f32 v228, v110, v111
	v_cvt_pk_f16_f32 v229, v112, v113
	v_mfma_f32_32x32x16_f16 v[18:33], v[222:225], v[6:9], v[18:33]
	v_add_u32_e32 v194, s13, v243
	v_mfma_f32_32x32x16_f16 v[18:33], v[226:229], v[10:13], v[18:33]
	s_branch .Lpeel_join

.Lpeel_join:
	v_cmp_ge_i32_e32 vcc, s18, v249
	s_mov_b64 s[8:9], 0
	s_and_saveexec_b64 s[2:3], vcc
	s_cbranch_execz .LBB1_148
	s_setprio 3
	v_cmp_gt_i32_e32 vcc, s12, v235
	s_and_b64 s[10:11], s[0:1], vcc
	ds_read_b128 v[82:85], v245 offset:32768
	ds_read_b128 v[86:89], v245 offset:32784
	ds_read_b128 v[90:93], v245 offset:32800
	ds_read_b128 v[94:97], v245 offset:32816
	ds_read_b128 v[98:101], v245 offset:32832
	ds_read_b128 v[102:105], v245 offset:32848
	ds_read_b128 v[106:109], v245 offset:32864
	ds_read_b128 v[110:113], v245 offset:32880
	ds_read_b128 v[114:117], v246 offset:0
	ds_read_b128 v[118:121], v246 offset:8192
	ds_read_b128 v[122:125], v246 offset:1024
	ds_read_b128 v[126:129], v246 offset:9216
	v_cvt_f32_i32_e32 v16, v234
	v_cvt_pk_f16_f32 v4, v66, v67
	v_cvt_pk_f16_f32 v5, v68, v69
	v_cvt_pk_f16_f32 v6, v70, v71
	v_cvt_pk_f16_f32 v7, v72, v73
	v_cvt_pk_f16_f32 v8, v74, v75
	v_cvt_pk_f16_f32 v9, v76, v77
	v_cvt_pk_f16_f32 v10, v78, v79
	v_cvt_pk_f16_f32 v11, v80, v81
	s_waitcnt lgkmcnt(8)
	v_pk_mul_f32 v[162:163], v[82:83], v[16:17] op_sel_hi:[1,0]
	v_pk_mul_f32 v[164:165], v[84:85], v[16:17] op_sel_hi:[1,0]
	v_pk_mul_f32 v[166:167], v[86:87], v[16:17] op_sel_hi:[1,0]
	v_pk_mul_f32 v[168:169], v[88:89], v[16:17] op_sel_hi:[1,0]
	v_pk_mul_f32 v[170:171], v[90:91], v[16:17] op_sel_hi:[1,0]
	v_pk_mul_f32 v[172:173], v[92:93], v[16:17] op_sel_hi:[1,0]
	v_pk_mul_f32 v[174:175], v[94:95], v[16:17] op_sel_hi:[1,0]
	v_pk_mul_f32 v[176:177], v[96:97], v[16:17] op_sel_hi:[1,0]
	ds_read_b128 v[130:133], v246 offset:2048
	ds_read_b128 v[134:137], v246 offset:10240
	ds_read_b128 v[138:141], v246 offset:3072
	ds_read_b128 v[142:145], v246 offset:11264
	s_waitcnt lgkmcnt(4)
	v_mfma_f32_32x32x16_f16 v[162:177], v[114:117], v[4:7], v[162:177]
	v_pk_mul_f32 v[146:147], v[98:99], v[16:17] op_sel_hi:[1,0]
	v_pk_mul_f32 v[148:149], v[100:101], v[16:17] op_sel_hi:[1,0]
	v_pk_mul_f32 v[150:151], v[102:103], v[16:17] op_sel_hi:[1,0]
	v_pk_mul_f32 v[152:153], v[104:105], v[16:17] op_sel_hi:[1,0]
	v_pk_mul_f32 v[154:155], v[106:107], v[16:17] op_sel_hi:[1,0]
	v_pk_mul_f32 v[156:157], v[108:109], v[16:17] op_sel_hi:[1,0]
	v_pk_mul_f32 v[158:159], v[110:111], v[16:17] op_sel_hi:[1,0]
	v_pk_mul_f32 v[160:161], v[112:113], v[16:17] op_sel_hi:[1,0]
	s_nop 1
	v_mfma_f32_32x32x16_f16 v[146:161], v[118:121], v[4:7], v[146:161]
	v_cvt_pk_f16_f32 v12, v50, v51
	v_cvt_pk_f16_f32 v13, v52, v53
	v_cvt_pk_f16_f32 v14, v54, v55
	v_cvt_pk_f16_f32 v15, v56, v57
	v_mfma_f32_32x32x16_f16 v[162:177], v[122:125], v[8:11], v[162:177]
	v_cvt_pk_f16_f32 v252, v58, v59
	v_cvt_pk_f16_f32 v253, v60, v61
	v_cvt_pk_f16_f32 v254, v62, v63
	v_cvt_pk_f16_f32 v255, v64, v65
	v_mfma_f32_32x32x16_f16 v[146:161], v[126:129], v[8:11], v[146:161]
	ds_read_b128 v[82:85], v246 offset:4096
	ds_read_b128 v[86:89], v246 offset:12288
	ds_read_b128 v[90:93], v246 offset:5120
	ds_read_b128 v[94:97], v246 offset:13312
	s_waitcnt lgkmcnt(4)
	v_mfma_f32_32x32x16_f16 v[162:177], v[130:133], v[12:15], v[162:177]
	v_cvt_pk_f16_f32 v4, v34, v35
	v_cvt_pk_f16_f32 v5, v36, v37
	v_mfma_f32_32x32x16_f16 v[146:161], v[134:137], v[12:15], v[146:161]
	v_cvt_pk_f16_f32 v6, v38, v39
	v_cvt_pk_f16_f32 v7, v40, v41
	v_mfma_f32_32x32x16_f16 v[162:177], v[138:141], v[252:255], v[162:177]
	v_cvt_pk_f16_f32 v8, v42, v43
	v_cvt_pk_f16_f32 v9, v44, v45
	v_mfma_f32_32x32x16_f16 v[146:161], v[142:145], v[252:255], v[146:161]
	v_cvt_pk_f16_f32 v10, v46, v47
	v_cvt_pk_f16_f32 v11, v48, v49
	ds_read_b128 v[98:101], v246 offset:6144
	ds_read_b128 v[102:105], v246 offset:14336
	ds_read_b128 v[106:109], v246 offset:7168
	ds_read_b128 v[110:113], v246 offset:15360
	s_waitcnt lgkmcnt(4)
	v_mfma_f32_32x32x16_f16 v[162:177], v[82:85], v[4:7], v[162:177]
	v_cvt_pk_f16_f32 v12, v18, v19
	v_cvt_pk_f16_f32 v13, v20, v21
	v_mfma_f32_32x32x16_f16 v[146:161], v[86:89], v[4:7], v[146:161]
	v_cvt_pk_f16_f32 v14, v22, v23
	v_cvt_pk_f16_f32 v15, v24, v25
	v_mfma_f32_32x32x16_f16 v[162:177], v[90:93], v[8:11], v[162:177]
	v_cvt_pk_f16_f32 v252, v26, v27
	v_cvt_pk_f16_f32 v253, v28, v29
	v_mfma_f32_32x32x16_f16 v[146:161], v[94:97], v[8:11], v[146:161]
	v_cvt_pk_f16_f32 v254, v30, v31
	v_cvt_pk_f16_f32 v255, v32, v33
	ds_read_b128 v[18:21], v246 offset:16384
	ds_read_b128 v[22:25], v246 offset:17408
	ds_read_b128 v[26:29], v246 offset:18432
	ds_read_b128 v[30:33], v246 offset:19456
	s_waitcnt lgkmcnt(4)
	v_mfma_f32_32x32x16_f16 v[162:177], v[98:101], v[12:15], v[162:177]
	v_mfma_f32_32x32x16_f16 v[146:161], v[102:105], v[12:15], v[146:161]
	v_mfma_f32_32x32x16_f16 v[162:177], v[106:109], v[252:255], v[162:177]
	v_mfma_f32_32x32x16_f16 v[146:161], v[110:113], v[252:255], v[146:161]
	ds_read_b128 v[130:133], v247 offset:33024
	ds_read_b128 v[134:137], v247 offset:33040
	ds_read_b128 v[138:141], v247 offset:33056
	ds_read_b128 v[142:145], v247 offset:33072
	ds_read_b128 v[114:117], v247 offset:33088
	ds_read_b128 v[118:121], v247 offset:33104
	ds_read_b128 v[122:125], v247 offset:33120
	ds_read_b128 v[126:129], v247 offset:33136
	s_nop 2
	v_cvt_pk_f16_f32 v4, v162, v163
	v_cvt_pk_f16_f32 v5, v164, v165
	v_cvt_pk_f16_f32 v6, v166, v167
	v_cvt_pk_f16_f32 v7, v168, v169
	v_cvt_pk_f16_f32 v8, v170, v171
	v_cvt_pk_f16_f32 v9, v172, v173
	v_cvt_pk_f16_f32 v10, v174, v175
	v_cvt_pk_f16_f32 v11, v176, v177
	v_cvt_pk_f16_f32 v12, v146, v147
	v_cvt_pk_f16_f32 v13, v148, v149
	v_cvt_pk_f16_f32 v14, v150, v151
	v_cvt_pk_f16_f32 v15, v152, v153
	v_cvt_pk_f16_f32 v252, v154, v155
	v_cvt_pk_f16_f32 v253, v156, v157
	v_cvt_pk_f16_f32 v254, v158, v159
	v_cvt_pk_f16_f32 v255, v160, v161
	s_waitcnt lgkmcnt(4)
	ds_read_b128 v[34:37], v246 offset:20480
	ds_read_b128 v[38:41], v246 offset:21504
	ds_read_b128 v[42:45], v246 offset:22528
	ds_read_b128 v[46:49], v246 offset:23552
	v_mfma_f32_32x32x16_f16 v[130:145], v[18:21], v[4:7], v[130:145]
	v_mfma_f32_32x32x16_f16 v[130:145], v[22:25], v[8:11], v[130:145]
	v_mfma_f32_32x32x16_f16 v[130:145], v[26:29], v[12:15], v[130:145]
	v_mfma_f32_32x32x16_f16 v[130:145], v[30:33], v[252:255], v[130:145]
	ds_read_b128 v[146:149], v247 offset:33536
	ds_read_b128 v[150:153], v247 offset:33552
	ds_read_b128 v[154:157], v247 offset:33568
	ds_read_b128 v[158:161], v247 offset:33584
	s_waitcnt lgkmcnt(4)
	ds_read_b128 v[98:101], v247 offset:33152
	ds_read_b128 v[102:105], v247 offset:33168
	ds_read_b128 v[106:109], v247 offset:33184
	ds_read_b128 v[110:113], v247 offset:33200
	ds_read_b128 v[50:53], v246 offset:24576
	ds_read_b128 v[54:57], v246 offset:25600
	ds_read_b128 v[58:61], v246 offset:26624
	ds_read_b128 v[62:65], v246 offset:27648
	v_mfma_f32_32x32x16_f16 v[114:129], v[34:37], v[4:7], v[114:129]
	v_exp_f32_e32 v130, v130
	v_exp_f32_e32 v131, v131
	v_exp_f32_e32 v132, v132
	v_exp_f32_e32 v133, v133
	v_exp_f32_e32 v134, v134
	v_exp_f32_e32 v135, v135
	v_exp_f32_e32 v136, v136
	v_exp_f32_e32 v137, v137
	v_mfma_f32_32x32x16_f16 v[114:129], v[38:41], v[8:11], v[114:129]
	v_exp_f32_e32 v138, v138
	v_exp_f32_e32 v139, v139
	v_exp_f32_e32 v140, v140
	v_exp_f32_e32 v141, v141
	v_exp_f32_e32 v142, v142
	v_exp_f32_e32 v143, v143
	v_exp_f32_e32 v144, v144
	v_exp_f32_e32 v145, v145
	v_mfma_f32_32x32x16_f16 v[114:129], v[42:45], v[12:15], v[114:129]
	v_pk_add_f32 v[130:131], v[130:131], s[82:83]
	v_pk_add_f32 v[132:133], v[132:133], s[82:83]
	v_pk_add_f32 v[134:135], v[134:135], s[82:83]
	v_pk_add_f32 v[136:137], v[136:137], s[82:83]
	v_pk_add_f32 v[138:139], v[138:139], s[82:83]
	v_pk_add_f32 v[140:141], v[140:141], s[82:83]
	v_pk_add_f32 v[142:143], v[142:143], s[82:83]
	v_pk_add_f32 v[144:145], v[144:145], s[82:83]
	v_mfma_f32_32x32x16_f16 v[114:129], v[46:49], v[252:255], v[114:129]
	v_rcp_f32_e32 v130, v130
	v_rcp_f32_e32 v131, v131
	v_rcp_f32_e32 v132, v132
	v_rcp_f32_e32 v133, v133
	v_rcp_f32_e32 v134, v134
	v_rcp_f32_e32 v135, v135
	v_rcp_f32_e32 v136, v136
	v_rcp_f32_e32 v137, v137
	v_rcp_f32_e32 v138, v138
	v_rcp_f32_e32 v139, v139
	v_rcp_f32_e32 v140, v140
	v_rcp_f32_e32 v141, v141
	v_rcp_f32_e32 v142, v142
	v_rcp_f32_e32 v143, v143
	v_rcp_f32_e32 v144, v144
	v_rcp_f32_e32 v145, v145
	s_waitcnt lgkmcnt(8)
	ds_read_b128 v[162:165], v247 offset:33600
	ds_read_b128 v[166:169], v247 offset:33616
	ds_read_b128 v[170:173], v247 offset:33632
	ds_read_b128 v[174:177], v247 offset:33648
	v_mul_f32_e32 v3, v146, v130
	v_mul_f32_e32 v16, v147, v131
	v_mul_f32_e32 v17, v148, v132
	v_fmac_f32_e32 v3, v149, v133
	v_fmac_f32_e32 v16, v150, v134
	v_fmac_f32_e32 v17, v151, v135
	v_fmac_f32_e32 v3, v152, v136
	v_fmac_f32_e32 v16, v153, v137
	v_fmac_f32_e32 v17, v154, v138
	v_fmac_f32_e32 v3, v155, v139
	v_fmac_f32_e32 v16, v156, v140
	v_fmac_f32_e32 v17, v157, v141
	v_fmac_f32_e32 v3, v158, v142
	v_fmac_f32_e32 v16, v159, v143
	v_fmac_f32_e32 v17, v160, v144
	v_fmac_f32_e32 v3, v161, v145
	s_waitcnt lgkmcnt(4)
	ds_read_b128 v[82:85], v247 offset:33216
	ds_read_b128 v[86:89], v247 offset:33232
	ds_read_b128 v[90:93], v247 offset:33248
	ds_read_b128 v[94:97], v247 offset:33264
	ds_read_b128 v[66:69], v246 offset:28672
	ds_read_b128 v[70:73], v246 offset:29696
	ds_read_b128 v[74:77], v246 offset:30720
	ds_read_b128 v[78:81], v246 offset:31744
	v_mfma_f32_32x32x16_f16 v[98:113], v[50:53], v[4:7], v[98:113]
	v_exp_f32_e32 v114, v114
	v_exp_f32_e32 v115, v115
	v_exp_f32_e32 v116, v116
	v_exp_f32_e32 v117, v117
	v_exp_f32_e32 v118, v118
	v_exp_f32_e32 v119, v119
	v_exp_f32_e32 v120, v120
	v_exp_f32_e32 v121, v121
	v_mfma_f32_32x32x16_f16 v[98:113], v[54:57], v[8:11], v[98:113]
	v_exp_f32_e32 v122, v122
	v_exp_f32_e32 v123, v123
	v_exp_f32_e32 v124, v124
	v_exp_f32_e32 v125, v125
	v_exp_f32_e32 v126, v126
	v_exp_f32_e32 v127, v127
	v_exp_f32_e32 v128, v128
	v_exp_f32_e32 v129, v129
	v_mfma_f32_32x32x16_f16 v[98:113], v[58:61], v[12:15], v[98:113]
	v_pk_add_f32 v[114:115], v[114:115], s[82:83]
	v_pk_add_f32 v[116:117], v[116:117], s[82:83]
	v_pk_add_f32 v[118:119], v[118:119], s[82:83]
	v_pk_add_f32 v[120:121], v[120:121], s[82:83]
	v_pk_add_f32 v[122:123], v[122:123], s[82:83]
	v_pk_add_f32 v[124:125], v[124:125], s[82:83]
	v_pk_add_f32 v[126:127], v[126:127], s[82:83]
	v_pk_add_f32 v[128:129], v[128:129], s[82:83]
	v_mfma_f32_32x32x16_f16 v[98:113], v[62:65], v[252:255], v[98:113]
	v_rcp_f32_e32 v114, v114
	v_rcp_f32_e32 v115, v115
	v_rcp_f32_e32 v116, v116
	v_rcp_f32_e32 v117, v117
	v_rcp_f32_e32 v118, v118
	v_rcp_f32_e32 v119, v119
	v_rcp_f32_e32 v120, v120
	v_rcp_f32_e32 v121, v121
	v_rcp_f32_e32 v122, v122
	v_rcp_f32_e32 v123, v123
	v_rcp_f32_e32 v124, v124
	v_rcp_f32_e32 v125, v125
	v_rcp_f32_e32 v126, v126
	v_rcp_f32_e32 v127, v127
	v_rcp_f32_e32 v128, v128
	v_rcp_f32_e32 v129, v129
	s_waitcnt lgkmcnt(8)
	ds_read_b128 v[18:21], v247 offset:33664
	ds_read_b128 v[22:25], v247 offset:33680
	ds_read_b128 v[26:29], v247 offset:33696
	ds_read_b128 v[30:33], v247 offset:33712
	v_fmac_f32_e32 v3, v162, v114
	v_fmac_f32_e32 v16, v163, v115
	v_fmac_f32_e32 v17, v164, v116
	v_fmac_f32_e32 v3, v165, v117
	v_fmac_f32_e32 v16, v166, v118
	v_fmac_f32_e32 v17, v167, v119
	v_fmac_f32_e32 v3, v168, v120
	v_fmac_f32_e32 v16, v169, v121
	v_fmac_f32_e32 v17, v170, v122
	v_fmac_f32_e32 v3, v171, v123
	v_fmac_f32_e32 v16, v172, v124
	v_fmac_f32_e32 v17, v173, v125
	v_fmac_f32_e32 v3, v174, v126
	v_fmac_f32_e32 v16, v175, v127
	v_fmac_f32_e32 v17, v176, v128
	v_fmac_f32_e32 v3, v177, v129
	s_waitcnt lgkmcnt(4)
	ds_read_b128 v[146:149], v247 offset:33728
	ds_read_b128 v[150:153], v247 offset:33744
	ds_read_b128 v[154:157], v247 offset:33760
	ds_read_b128 v[158:161], v247 offset:33776
	v_mfma_f32_32x32x16_f16 v[82:97], v[66:69], v[4:7], v[82:97]
	v_exp_f32_e32 v98, v98
	v_exp_f32_e32 v99, v99
	v_exp_f32_e32 v100, v100
	v_exp_f32_e32 v101, v101
	v_exp_f32_e32 v102, v102
	v_exp_f32_e32 v103, v103
	v_exp_f32_e32 v104, v104
	v_exp_f32_e32 v105, v105
	v_mfma_f32_32x32x16_f16 v[82:97], v[70:73], v[8:11], v[82:97]
	v_exp_f32_e32 v106, v106
	v_exp_f32_e32 v107, v107
	v_exp_f32_e32 v108, v108
	v_exp_f32_e32 v109, v109
	v_exp_f32_e32 v110, v110
	v_exp_f32_e32 v111, v111
	v_exp_f32_e32 v112, v112
	v_exp_f32_e32 v113, v113
	v_mfma_f32_32x32x16_f16 v[82:97], v[74:77], v[12:15], v[82:97]
	v_pk_add_f32 v[98:99], v[98:99], s[82:83]
	v_pk_add_f32 v[100:101], v[100:101], s[82:83]
	v_pk_add_f32 v[102:103], v[102:103], s[82:83]
	v_pk_add_f32 v[104:105], v[104:105], s[82:83]
	v_pk_add_f32 v[106:107], v[106:107], s[82:83]
	v_pk_add_f32 v[108:109], v[108:109], s[82:83]
	v_pk_add_f32 v[110:111], v[110:111], s[82:83]
	v_pk_add_f32 v[112:113], v[112:113], s[82:83]
	v_mfma_f32_32x32x16_f16 v[82:97], v[78:81], v[252:255], v[82:97]
	v_rcp_f32_e32 v98, v98
	v_rcp_f32_e32 v99, v99
	v_rcp_f32_e32 v100, v100
	v_rcp_f32_e32 v101, v101
	v_rcp_f32_e32 v102, v102
	v_rcp_f32_e32 v103, v103
	v_rcp_f32_e32 v104, v104
	v_rcp_f32_e32 v105, v105
	v_rcp_f32_e32 v106, v106
	v_rcp_f32_e32 v107, v107
	v_rcp_f32_e32 v108, v108
	v_rcp_f32_e32 v109, v109
	v_rcp_f32_e32 v110, v110
	v_rcp_f32_e32 v111, v111
	v_rcp_f32_e32 v112, v112
	v_rcp_f32_e32 v113, v113
	s_waitcnt lgkmcnt(4)
	v_fmac_f32_e32 v3, v18, v98
	v_fmac_f32_e32 v16, v19, v99
	v_fmac_f32_e32 v17, v20, v100
	v_fmac_f32_e32 v3, v21, v101
	v_fmac_f32_e32 v16, v22, v102
	v_fmac_f32_e32 v17, v23, v103
	v_fmac_f32_e32 v3, v24, v104
	v_fmac_f32_e32 v16, v25, v105
	v_fmac_f32_e32 v17, v26, v106
	v_fmac_f32_e32 v3, v27, v107
	v_fmac_f32_e32 v16, v28, v108
	v_fmac_f32_e32 v17, v29, v109
	v_fmac_f32_e32 v3, v30, v110
	v_fmac_f32_e32 v16, v31, v111
	v_fmac_f32_e32 v17, v32, v112
	v_fmac_f32_e32 v3, v33, v113
	v_exp_f32_e32 v82, v82
	v_exp_f32_e32 v83, v83
	v_exp_f32_e32 v84, v84
	v_exp_f32_e32 v85, v85
	v_exp_f32_e32 v86, v86
	v_exp_f32_e32 v87, v87
	v_exp_f32_e32 v88, v88
	v_exp_f32_e32 v89, v89
	v_exp_f32_e32 v90, v90
	v_exp_f32_e32 v91, v91
	v_exp_f32_e32 v92, v92
	v_exp_f32_e32 v93, v93
	v_exp_f32_e32 v94, v94
	v_exp_f32_e32 v95, v95
	v_exp_f32_e32 v96, v96
	v_exp_f32_e32 v97, v97
	v_pk_add_f32 v[82:83], v[82:83], s[82:83]
	v_pk_add_f32 v[84:85], v[84:85], s[82:83]
	v_pk_add_f32 v[86:87], v[86:87], s[82:83]
	v_pk_add_f32 v[88:89], v[88:89], s[82:83]
	v_pk_add_f32 v[90:91], v[90:91], s[82:83]
	v_pk_add_f32 v[92:93], v[92:93], s[82:83]
	v_pk_add_f32 v[94:95], v[94:95], s[82:83]
	v_pk_add_f32 v[96:97], v[96:97], s[82:83]
	v_rcp_f32_e32 v82, v82
	v_rcp_f32_e32 v83, v83
	v_rcp_f32_e32 v84, v84
	v_rcp_f32_e32 v85, v85
	v_rcp_f32_e32 v86, v86
	v_rcp_f32_e32 v87, v87
	v_rcp_f32_e32 v88, v88
	v_rcp_f32_e32 v89, v89
	v_rcp_f32_e32 v90, v90
	v_rcp_f32_e32 v91, v91
	v_rcp_f32_e32 v92, v92
	v_rcp_f32_e32 v93, v93
	v_rcp_f32_e32 v94, v94
	v_rcp_f32_e32 v95, v95
	v_rcp_f32_e32 v96, v96
	v_rcp_f32_e32 v97, v97
	s_waitcnt lgkmcnt(0)
	v_fmac_f32_e32 v3, v146, v82
	v_fmac_f32_e32 v16, v147, v83
	v_fmac_f32_e32 v17, v148, v84
	v_fmac_f32_e32 v3, v149, v85
	v_fmac_f32_e32 v16, v150, v86
	v_fmac_f32_e32 v17, v151, v87
	v_fmac_f32_e32 v3, v152, v88
	v_fmac_f32_e32 v16, v153, v89
	v_fmac_f32_e32 v17, v154, v90
	v_fmac_f32_e32 v3, v155, v91
	v_fmac_f32_e32 v16, v156, v92
	v_fmac_f32_e32 v17, v157, v93
	v_fmac_f32_e32 v3, v158, v94
	v_fmac_f32_e32 v16, v159, v95
	v_fmac_f32_e32 v17, v160, v96
	v_fmac_f32_e32 v3, v161, v97
	v_add_f32_e32 v3, v3, v16
	v_add_f32_e32 v3, v3, v17
	v_mov_b32_e32 v4, v3
	s_nop 1
	v_permlane32_swap_b32_e32 v4, v3
	s_and_saveexec_b64 s[8:9], s[10:11]
	s_cbranch_execz .LBB1_156
	s_waitcnt vmcnt(0)
	v_mul_f32_e32 v5, 0x40549a78, v238
	v_exp_f32_e32 v5, v5
	v_add_f32_e32 v3, v3, v4
	v_ashrrev_i32_e32 v7, 31, v235
	v_mov_b32_e32 v6, v235
	v_add_f32_e32 v3, v239, v3
	v_lshl_add_u64 v[6:7], v[6:7], 2, s[52:53]
	v_mul_f32_e32 v3, v5, v3
	global_store_dword v[6:7], v3, off
